# gate-up GEMM epilogue: per-column weight steps prefetched before the K-loop; drain wait moved to first store (6 phases)
# speedup vs baseline: 1.0058x; 1.0020x over previous
;     __device__ __forceinline__ void operator()(const f32x4 (&acc)[2][2][4][2], const Unit& u, int wr, int wc, int fr, int fq) const {
;     ...
;         for (int n = 0; n < 2; ++n) { cg[n] = IN8 ? *(const f32x4*)(cstep + u.pn * BM + wc * 32 + 8 * fq + 4 * n) : (f32x4){1.f, 1.f, 1.f, 1.f}; cu[n] = IN8 ? *(const f32x4*)(cstep + u.pn * BM + HALF + wc * 32 + 8 * fq + 4 * n) : (f32x4){1.f, 1.f, 1.f, 1.f}; }
;     ...
; #pragma unroll
;     for (int a = 0; a < 2; ++a)
; #pragma unroll
;         for (int b = 0; b < 2; ++b)
; #pragma unroll
;             for (int m = 0; m < 4; ++m)
; #pragma unroll
;                 for (int n = 0; n < 2; ++n) acc[a][b][m][n] = (f32x4){0.f, 0.f, 0.f, 0.f};
;     bf16x8 At[4][2], B0[2][2], B1[2][2];
;     i32x8 At8[4], B08[2], B18[2];
;     const char* cA = (const char*)g.A + (size_t)cur.pm * tstepA; const char* cB = (const char*)g.Bt + (size_t)cur.pn * tstepB;
.LBB0_225:
	s_ashr_i32 s17, s16, 31
	s_lshl_b64 s[18:19], s[16:17], 19
	s_add_u32 s18, s37, s18
	s_addc_u32 s19, s38, s19
	s_ashr_i32 s15, s14, 31
	s_lshl_b64 s[20:21], s[14:15], 19
	s_add_u32 s20, s39, s20
	v_mov_b32_e32 v129, 0
	s_addc_u32 s21, s40, s21
	s_andn2_b64 vcc, exec, s[10:11]
	v_mov_b32_e32 v128, v129
	v_mov_b32_e32 v127, v129
	v_mov_b32_e32 v126, v129
	v_mov_b32_e32 v121, v129
	v_mov_b32_e32 v120, v129
	v_mov_b32_e32 v119, v129
	v_mov_b32_e32 v118, v129
	v_mov_b32_e32 v113, v129
	v_mov_b32_e32 v112, v129
	v_mov_b32_e32 v111, v129
	v_mov_b32_e32 v110, v129
	v_mov_b32_e32 v105, v129
	v_mov_b32_e32 v104, v129
	v_mov_b32_e32 v103, v129
	v_mov_b32_e32 v102, v129
	v_mov_b32_e32 v97, v129
	v_mov_b32_e32 v96, v129
	v_mov_b32_e32 v95, v129
	v_mov_b32_e32 v94, v129
	v_mov_b32_e32 v89, v129
	v_mov_b32_e32 v88, v129
	v_mov_b32_e32 v87, v129
	v_mov_b32_e32 v86, v129
	v_mov_b32_e32 v81, v129
	v_mov_b32_e32 v80, v129
	v_mov_b32_e32 v79, v129
	v_mov_b32_e32 v78, v129
	v_mov_b32_e32 v73, v129
	v_mov_b32_e32 v72, v129
	v_mov_b32_e32 v71, v129
	v_mov_b32_e32 v70, v129
	v_mov_b32_e32 v125, v129
	v_mov_b32_e32 v124, v129
	v_mov_b32_e32 v123, v129
	v_mov_b32_e32 v122, v129
	v_mov_b32_e32 v117, v129
	v_mov_b32_e32 v116, v129
	v_mov_b32_e32 v115, v129
	v_mov_b32_e32 v114, v129
	v_mov_b32_e32 v109, v129
	v_mov_b32_e32 v108, v129
	v_mov_b32_e32 v107, v129
	v_mov_b32_e32 v106, v129
	v_mov_b32_e32 v101, v129
	v_mov_b32_e32 v100, v129
	v_mov_b32_e32 v99, v129
	v_mov_b32_e32 v98, v129
	v_mov_b32_e32 v93, v129
	v_mov_b32_e32 v92, v129
	v_mov_b32_e32 v91, v129
	v_mov_b32_e32 v90, v129
	v_mov_b32_e32 v85, v129
	v_mov_b32_e32 v84, v129
	v_mov_b32_e32 v83, v129
	v_mov_b32_e32 v82, v129
	v_mov_b32_e32 v77, v129
	v_mov_b32_e32 v76, v129
	v_mov_b32_e32 v75, v129
	v_mov_b32_e32 v74, v129
	v_mov_b32_e32 v69, v129
	v_mov_b32_e32 v68, v129
	v_mov_b32_e32 v67, v129
	v_mov_b32_e32 v66, v129
	v_mov_b32_e32 v65, v129
	v_mov_b32_e32 v64, v129
	v_mov_b32_e32 v63, v129
	v_mov_b32_e32 v62, v129
	v_mov_b32_e32 v57, v129
	v_mov_b32_e32 v56, v129
	v_mov_b32_e32 v55, v129
	v_mov_b32_e32 v54, v129
	v_mov_b32_e32 v49, v129
	v_mov_b32_e32 v48, v129
	v_mov_b32_e32 v47, v129
	v_mov_b32_e32 v46, v129
	v_mov_b32_e32 v41, v129
	v_mov_b32_e32 v40, v129
	v_mov_b32_e32 v39, v129
	v_mov_b32_e32 v38, v129
	v_mov_b32_e32 v33, v129
	v_mov_b32_e32 v32, v129
	v_mov_b32_e32 v31, v129
	v_mov_b32_e32 v30, v129
	v_mov_b32_e32 v25, v129
	v_mov_b32_e32 v24, v129
	v_mov_b32_e32 v23, v129
	v_mov_b32_e32 v22, v129
	v_mov_b32_e32 v17, v129
	v_mov_b32_e32 v16, v129
	v_mov_b32_e32 v15, v129
	v_mov_b32_e32 v14, v129
	v_mov_b32_e32 v9, v129
	v_mov_b32_e32 v8, v129
	v_mov_b32_e32 v7, v129
	v_mov_b32_e32 v6, v129
	v_mov_b32_e32 v61, v129
	v_mov_b32_e32 v60, v129
	v_mov_b32_e32 v59, v129
	v_mov_b32_e32 v58, v129
	v_mov_b32_e32 v53, v129
	v_mov_b32_e32 v52, v129
	v_mov_b32_e32 v51, v129
	v_mov_b32_e32 v50, v129
	v_mov_b32_e32 v45, v129
	v_mov_b32_e32 v44, v129
	v_mov_b32_e32 v43, v129
	v_mov_b32_e32 v42, v129
	v_mov_b32_e32 v37, v129
	v_mov_b32_e32 v36, v129
	v_mov_b32_e32 v35, v129
	v_mov_b32_e32 v34, v129
	v_mov_b32_e32 v29, v129
	v_mov_b32_e32 v28, v129
	v_mov_b32_e32 v27, v129
	v_mov_b32_e32 v26, v129
	v_mov_b32_e32 v21, v129
	v_mov_b32_e32 v20, v129
	v_mov_b32_e32 v19, v129
	v_mov_b32_e32 v18, v129
	v_mov_b32_e32 v13, v129
	v_mov_b32_e32 v12, v129
	v_mov_b32_e32 v11, v129
	v_mov_b32_e32 v10, v129
	v_mov_b32_e32 v5, v129
	v_mov_b32_e32 v4, v129
	v_mov_b32_e32 v3, v129
	v_mov_b32_e32 v2, v129
	s_cbranch_vccnz .LBB0_228
	s_and_b64 s[28:29], s[0:1], exec
	s_cselect_b32 s15, s19, s27
	s_cselect_b32 s17, s18, s26
	s_cselect_b32 s64, s21, s25
	s_cselect_b32 s65, s20, s24
	s_add_u32 s66, s24, 0x100
	s_addc_u32 s67, s25, 0
	s_add_u32 s24, s26, 0x40080
	s_addc_u32 s25, s27, 0
	s_mov_b32 s26, 0
	v_mov_b32_e32 v2, 0
	v_mov_b32_e32 v3, 0
	v_mov_b32_e32 v4, 0
	v_mov_b32_e32 v5, 0
	v_mov_b32_e32 v10, 0
	v_mov_b32_e32 v11, 0
	v_mov_b32_e32 v12, 0
	v_mov_b32_e32 v13, 0
	v_mov_b32_e32 v18, 0
	v_mov_b32_e32 v19, 0
	v_mov_b32_e32 v20, 0
	v_mov_b32_e32 v21, 0
	v_mov_b32_e32 v26, 0
	v_mov_b32_e32 v27, 0
	v_mov_b32_e32 v28, 0
	v_mov_b32_e32 v29, 0
	v_mov_b32_e32 v34, 0
	v_mov_b32_e32 v35, 0
	v_mov_b32_e32 v36, 0
	v_mov_b32_e32 v37, 0
	v_mov_b32_e32 v42, 0
	v_mov_b32_e32 v43, 0
	v_mov_b32_e32 v44, 0
	v_mov_b32_e32 v45, 0
	v_mov_b32_e32 v50, 0
	v_mov_b32_e32 v51, 0
	v_mov_b32_e32 v52, 0
	v_mov_b32_e32 v53, 0
	v_mov_b32_e32 v58, 0
	v_mov_b32_e32 v59, 0
	v_mov_b32_e32 v60, 0
	v_mov_b32_e32 v61, 0
	v_mov_b32_e32 v6, 0
	v_mov_b32_e32 v7, 0
	v_mov_b32_e32 v8, 0
	v_mov_b32_e32 v9, 0
	v_mov_b32_e32 v14, 0
	v_mov_b32_e32 v15, 0
	v_mov_b32_e32 v16, 0
	v_mov_b32_e32 v17, 0
	v_mov_b32_e32 v22, 0
	v_mov_b32_e32 v23, 0
	v_mov_b32_e32 v24, 0
	v_mov_b32_e32 v25, 0
	v_mov_b32_e32 v30, 0
	v_mov_b32_e32 v31, 0
	v_mov_b32_e32 v32, 0
	v_mov_b32_e32 v33, 0
	v_mov_b32_e32 v38, 0
	v_mov_b32_e32 v39, 0
	v_mov_b32_e32 v40, 0
	v_mov_b32_e32 v41, 0
	v_mov_b32_e32 v46, 0
	v_mov_b32_e32 v47, 0
	v_mov_b32_e32 v48, 0
	v_mov_b32_e32 v49, 0
	v_mov_b32_e32 v54, 0
	v_mov_b32_e32 v55, 0
	v_mov_b32_e32 v56, 0
	v_mov_b32_e32 v57, 0
	v_mov_b32_e32 v62, 0
	v_mov_b32_e32 v63, 0
	v_mov_b32_e32 v64, 0
	v_mov_b32_e32 v65, 0
	v_mov_b32_e32 v66, 0
	v_mov_b32_e32 v67, 0
	v_mov_b32_e32 v68, 0
	v_mov_b32_e32 v69, 0
	v_mov_b32_e32 v74, 0
	v_mov_b32_e32 v75, 0
	v_mov_b32_e32 v76, 0
	v_mov_b32_e32 v77, 0
	v_mov_b32_e32 v82, 0
	v_mov_b32_e32 v83, 0
	v_mov_b32_e32 v84, 0
	v_mov_b32_e32 v85, 0
	v_mov_b32_e32 v90, 0
	v_mov_b32_e32 v91, 0
	v_mov_b32_e32 v92, 0
	v_mov_b32_e32 v93, 0
	v_mov_b32_e32 v98, 0
	v_mov_b32_e32 v99, 0
	v_mov_b32_e32 v100, 0
	v_mov_b32_e32 v101, 0
	v_mov_b32_e32 v106, 0
	v_mov_b32_e32 v107, 0
	v_mov_b32_e32 v108, 0
	v_mov_b32_e32 v109, 0
	v_mov_b32_e32 v114, 0
	v_mov_b32_e32 v115, 0
	v_mov_b32_e32 v116, 0
	v_mov_b32_e32 v117, 0
	v_mov_b32_e32 v122, 0
	v_mov_b32_e32 v123, 0
	v_mov_b32_e32 v124, 0
	v_mov_b32_e32 v125, 0
	v_mov_b32_e32 v70, 0
	v_mov_b32_e32 v71, 0
	v_mov_b32_e32 v72, 0
	v_mov_b32_e32 v73, 0
	v_mov_b32_e32 v78, 0
	v_mov_b32_e32 v79, 0
	v_mov_b32_e32 v80, 0
	v_mov_b32_e32 v81, 0
	v_mov_b32_e32 v86, 0
	v_mov_b32_e32 v87, 0
	v_mov_b32_e32 v88, 0
	v_mov_b32_e32 v89, 0
	v_mov_b32_e32 v94, 0
	v_mov_b32_e32 v95, 0
	v_mov_b32_e32 v96, 0
	v_mov_b32_e32 v97, 0
	v_mov_b32_e32 v102, 0
	v_mov_b32_e32 v103, 0
	v_mov_b32_e32 v104, 0
	v_mov_b32_e32 v105, 0
	v_mov_b32_e32 v110, 0
	v_mov_b32_e32 v111, 0
	v_mov_b32_e32 v112, 0
	v_mov_b32_e32 v113, 0
	v_mov_b32_e32 v118, 0
	v_mov_b32_e32 v119, 0
	v_mov_b32_e32 v120, 0
	v_mov_b32_e32 v121, 0
	v_mov_b32_e32 v126, 0
	v_mov_b32_e32 v127, 0
	v_mov_b32_e32 v128, 0
	v_mov_b32_e32 v129, 0
	s_lshl_b32 s98, s63, 8
	s_ashr_i32 s99, s98, 31
	v_lshl_add_u64 v[242:243], s[98:99], 2, v[154:155]
	global_load_dwordx4 v[226:229], v[242:243], off
	global_load_dwordx4 v[230:233], v[242:243], off offset:512
	global_load_dwordx4 v[234:237], v[242:243], off offset:16
	global_load_dwordx4 v[238:241], v[242:243], off offset:528

; __device__ __forceinline__ float fast_sigmoid(float x) { return __builtin_amdgcn_rcpf(1.0f + __expf(-x)); }
;     __device__ __forceinline__ void operator()(const f32x4 (&acc)[2][2][4][2], const Unit& u, int wr, int wc, int fr, int fq) const {
;         const int row0 = u.pm * BM + wr * 64 + fr, col0 = u.pn * HALF + wc * 32 + 8 * fq; const int sl = IN8 ? rt.slot(u.pm) : 0;
;         f32x4 cg[2], cu[2];
; #pragma unroll
;         for (int n = 0; n < 2; ++n) { cg[n] = IN8 ? *(const f32x4*)(cstep + u.pn * BM + wc * 32 + 8 * fq + 4 * n) : (f32x4){1.f, 1.f, 1.f, 1.f}; cu[n] = IN8 ? *(const f32x4*)(cstep + u.pn * BM + HALF + wc * 32 + 8 * fq + 4 * n) : (f32x4){1.f, 1.f, 1.f, 1.f}; }
; #pragma unroll
;         for (int ai = 0; ai < 2; ++ai)
; #pragma unroll
;             for (int m = 0; m < 4; ++m) { const size_t off = (size_t)(row0 + ai * HALF + m * 16) * ldc + col0;
;                 const float rs = IN8 ? rt.tab[sl * 256 + wr * 64 + ai * HALF + m * 16 + fr] : isc;
;                 const float rsn = rs * -1.4426950408889634f, rs2 = rs * rs; (void)rsn; (void)rs2;
;                 float o[8];
; #pragma unroll
;                 for (int n = 0; n < 2; ++n)
; #pragma unroll
;                     for (int e = 0; e < 4; ++e) { const float ga = acc[ai][0][m][n][e], ua = acc[ai][1][m][n][e];
;                         if (IN8) {
;                             const float gq = (float)__float_as_int(ga) * cg[n][e], uq = (float)__float_as_int(ua) * cu[n][e];
;                             const float sg = __builtin_amdgcn_rcpf(1.0f + __builtin_amdgcn_exp2f(gq * rsn));
;                             o[4 * n + e] = (gq * uq) * (sg * rs2); }
;                         else { const float g = ga * rs, up = ua * rs; o[4 * n + e] = g * fast_sigmoid(g) * up; } }
.LBB0_230:
	s_lshl_b32 s24, s63, 8
	s_ashr_i32 s25, s24, 31
	s_nop 0
	v_mov_b32_e32 v142, v226
	v_mov_b32_e32 v143, v227
	v_mov_b32_e32 v144, v228
	v_mov_b32_e32 v145, v229
	v_mov_b32_e32 v138, v230
	v_mov_b32_e32 v139, v231
	v_mov_b32_e32 v140, v232
	v_mov_b32_e32 v141, v233
	v_mov_b32_e32 v134, v234
	v_mov_b32_e32 v135, v235
	v_mov_b32_e32 v136, v236
	v_mov_b32_e32 v137, v237
	s_nop 0
	v_mov_b32_e32 v130, v238
	v_mov_b32_e32 v131, v239
	v_mov_b32_e32 v132, v240
	v_mov_b32_e32 v133, v241
	s_add_i32 s15, s34, 0x20204
	v_cvt_f32_i32_e32 v172, v118
	v_mov_b32_e32 v118, s15
	v_cvt_f32_i32_e32 v173, v119
	ds_read2_b32 v[118:119], v118 offset1:1
	s_add_i32 s17, s34, 0x2020c
	s_add_i32 s24, s34, 0x20214
	s_add_i32 s25, s34, 0x2021c
	v_mov_b32_e32 v169, s17
	v_mov_b32_e32 v171, s24
	v_mov_b32_e32 v178, s25
	ds_read2_b32 v[174:175], v169 offset1:1
	ds_read2_b32 v[176:177], v171 offset1:1
	ds_read_b32 v169, v178
	s_waitcnt lgkmcnt(0)
	v_cmp_eq_u32_e32 vcc, s22, v118
	v_cvt_f32_i32_e32 v127, v127
	v_cvt_f32_i32_e32 v126, v126
	v_cndmask_b32_e64 v118, 0, 1, vcc
	v_cmp_ne_u32_e32 vcc, s22, v119
	v_cvt_f32_i32_e32 v123, v123
	v_cvt_f32_i32_e32 v122, v122
	v_cndmask_b32_e32 v118, 2, v118, vcc
	v_cmp_ne_u32_e32 vcc, s22, v174
	v_cvt_f32_i32_e32 v129, v129
	v_cvt_f32_i32_e32 v128, v128
	v_cndmask_b32_e32 v118, 3, v118, vcc
	v_cmp_ne_u32_e32 vcc, s22, v175
	v_cvt_f32_i32_e32 v125, v125
	v_cvt_f32_i32_e32 v124, v124
	v_cndmask_b32_e32 v118, 4, v118, vcc
	v_cmp_ne_u32_e32 vcc, s22, v176
	v_cvt_f32_i32_e32 v121, v121
	v_cvt_f32_i32_e32 v120, v120
	v_cndmask_b32_e32 v118, 5, v118, vcc
	v_cmp_ne_u32_e32 vcc, s22, v177
	v_cvt_f32_i32_e32 v115, v115
	v_cvt_f32_i32_e32 v114, v114
	v_cndmask_b32_e32 v118, 6, v118, vcc
	v_cmp_ne_u32_e32 vcc, s22, v169
	v_cvt_f32_i32_e32 v117, v117
	v_cvt_f32_i32_e32 v116, v116
	v_cndmask_b32_e32 v118, 7, v118, vcc
	v_lshl_or_b32 v170, s63, 7, v165
	v_readfirstlane_b32 s15, v118
	v_lshl_add_u32 v168, s22, 8, v1
	v_ashrrev_i32_e32 v171, 31, v170
	v_lshl_add_u32 v118, s15, 10, v166
	ds_read2_b32 v[174:175], v118 offset1:16
	v_cvt_f32_i32_e32 v113, v113
	v_cvt_f32_i32_e32 v112, v112
	v_cvt_f32_i32_e32 v107, v107
	v_cvt_f32_i32_e32 v106, v106
	s_waitcnt lgkmcnt(0)
	v_mul_f32_e32 v119, 0xbfb8aa3b, v174
	v_mul_f32_e32 v174, v174, v174
	v_cvt_f32_i32_e32 v109, v109
	v_cvt_f32_i32_e32 v108, v108
	v_cvt_f32_i32_e32 v103, v103
	v_cvt_f32_i32_e32 v102, v102
	v_cvt_f32_i32_e32 v99, v99
	v_cvt_f32_i32_e32 v98, v98
	v_cvt_f32_i32_e32 v105, v105
	v_cvt_f32_i32_e32 v104, v104
	v_cvt_f32_i32_e32 v101, v101
	v_cvt_f32_i32_e32 v100, v100
	v_cvt_f32_i32_e32 v95, v95
	v_cvt_f32_i32_e32 v94, v94
	v_cvt_f32_i32_e32 v91, v91
	v_cvt_f32_i32_e32 v90, v90
	v_cvt_f32_i32_e32 v97, v97
	v_cvt_f32_i32_e32 v96, v96
	v_cvt_f32_i32_e32 v93, v93
	v_cvt_f32_i32_e32 v92, v92
	v_cvt_f32_i32_e32 v87, v87
	v_cvt_f32_i32_e32 v86, v86
	v_cvt_f32_i32_e32 v83, v83
	v_cvt_f32_i32_e32 v82, v82
	v_cvt_f32_i32_e32 v89, v89
	v_cvt_f32_i32_e32 v88, v88
	s_nop 0
	v_pk_mul_f32 v[126:127], v[142:143], v[126:127]
	v_pk_mul_f32 v[122:123], v[138:139], v[122:123]
	v_pk_mul_f32 v[128:129], v[144:145], v[128:129]
	v_pk_mul_f32 v[124:125], v[140:141], v[124:125]
	v_pk_mul_f32 v[172:173], v[134:135], v[172:173]
	v_pk_mul_f32 v[176:177], v[136:137], v[120:121]
	v_mul_f32_e32 v169, v126, v119
	v_mul_f32_e32 v178, v127, v119
	v_pk_mul_f32 v[120:121], v[126:127], v[122:123]
	v_mul_f32_e32 v126, v128, v119
	v_mul_f32_e32 v127, v129, v119
	v_pk_mul_f32 v[122:123], v[128:129], v[124:125]
	v_mul_f32_e32 v124, v172, v119
	v_mul_f32_e32 v125, v173, v119
	v_exp_f32_e32 v129, v169
	v_exp_f32_e32 v169, v178
	v_exp_f32_e32 v126, v126
	v_exp_f32_e32 v127, v127
	v_exp_f32_e32 v124, v124
	v_exp_f32_e32 v125, v125
	v_pk_mul_f32 v[114:115], v[130:131], v[114:115]
	v_mul_f32_e32 v128, v176, v119
	v_pk_mul_f32 v[114:115], v[172:173], v[114:115]
	v_exp_f32_e32 v172, v128
	v_add_f32_e32 v128, 1.0, v129
	v_add_f32_e32 v129, 1.0, v169
	v_add_f32_e32 v126, 1.0, v126
	v_add_f32_e32 v127, 1.0, v127
	v_add_f32_e32 v169, 1.0, v124
	v_add_f32_e32 v173, 1.0, v125
	v_rcp_f32_e32 v124, v128
	v_rcp_f32_e32 v125, v129
	v_rcp_f32_e32 v126, v126
	v_rcp_f32_e32 v127, v127
	v_rcp_f32_e32 v128, v169
	v_rcp_f32_e32 v129, v173
	v_mul_f32_e32 v119, v177, v119
	v_exp_f32_e32 v119, v119
	v_pk_mul_f32 v[124:125], v[174:175], v[124:125] op_sel_hi:[0,1]
	v_pk_mul_f32 v[126:127], v[174:175], v[126:127] op_sel_hi:[0,1]
	v_pk_mul_f32 v[120:121], v[120:121], v[124:125]
	v_pk_mul_f32 v[122:123], v[122:123], v[126:127]
	v_cvt_pk_bf16_f32 v120, v120, v121
	v_cvt_pk_bf16_f32 v121, v122, v123
	v_pk_mul_f32 v[122:123], v[174:175], v[128:129] op_sel_hi:[0,1]
	v_pk_mul_f32 v[114:115], v[114:115], v[122:123]
	v_add_f32_e32 v122, 1.0, v172
	v_add_f32_e32 v119, 1.0, v119
	v_rcp_f32_e32 v124, v122
	v_rcp_f32_e32 v125, v119
	v_cvt_pk_bf16_f32 v122, v114, v115
	v_pk_mul_f32 v[114:115], v[132:133], v[116:117]
	v_mul_f32_e32 v119, 0xbfb8aa3b, v175
	v_pk_mul_f32 v[114:115], v[176:177], v[114:115]
	v_pk_mul_f32 v[116:117], v[174:175], v[124:125] op_sel_hi:[0,1]
	v_cvt_f32_i32_e32 v125, v111
	v_cvt_f32_i32_e32 v124, v110
	v_pk_mul_f32 v[114:115], v[114:115], v[116:117]
	v_lshlrev_b64 v[110:111], 1, v[170:171]
	v_cvt_pk_bf16_f32 v123, v114, v115
	v_mov_b64_e32 v[114:115], s[6:7]
	v_mad_i64_i32 v[116:117], s[24:25], v168, s62, v[114:115]
	v_lshl_add_u64 v[116:117], v[116:117], 0, v[110:111]
	v_pk_mul_f32 v[124:125], v[142:143], v[124:125]
	s_waitcnt vmcnt(0)
; __device__ __forceinline__ float fast_sigmoid(float x) { return __builtin_amdgcn_rcpf(1.0f + __expf(-x)); }
;     __device__ __forceinline__ void operator()(const f32x4 (&acc)[2][2][4][2], const Unit& u, int wr, int wc, int fr, int fq) const {
;     ...
;             for (int m = 0; m < 4; ++m) { const size_t off = (size_t)(row0 + ai * HALF + m * 16) * ldc + col0;
;                 const float rs = IN8 ? rt.tab[sl * 256 + wr * 64 + ai * HALF + m * 16 + fr] : isc;
;                 const float rsn = rs * -1.4426950408889634f, rs2 = rs * rs; (void)rsn; (void)rs2;
;                 float o[8];
; #pragma unroll
;                 for (int n = 0; n < 2; ++n)
; #pragma unroll
;                     for (int e = 0; e < 4; ++e) { const float ga = acc[ai][0][m][n][e], ua = acc[ai][1][m][n][e];
;                         if (IN8) {
;                             const float gq = (float)__float_as_int(ga) * cg[n][e], uq = (float)__float_as_int(ua) * cu[n][e];
;                             const float sg = __builtin_amdgcn_rcpf(1.0f + __builtin_amdgcn_exp2f(gq * rsn));
;                             o[4 * n + e] = (gq * uq) * (sg * rs2); }
;                         else { const float g = ga * rs, up = ua * rs; o[4 * n + e] = g * fast_sigmoid(g) * up; } }
;                 if (F8) { unsigned w0 = 0u, w1 = 0u;
; #pragma unroll
;                     for (int e = 0; e < 8; ++e) o[e] = __builtin_amdgcn_fmed3f(o[e] * H8_SCALE, -448.0f, 448.0f);
;                     w0 = __builtin_amdgcn_cvt_pk_fp8_f32(o[0], o[1], w0, false); w0 = __builtin_amdgcn_cvt_pk_fp8_f32(o[2], o[3], w0, true);
;                     w1 = __builtin_amdgcn_cvt_pk_fp8_f32(o[4], o[5], w1, false); w1 = __builtin_amdgcn_cvt_pk_fp8_f32(o[6], o[7], w1, true);
;                     typedef unsigned u32x2_ __attribute__((ext_vector_type(2))); *(u32x2_*)((unsigned char*)O + off) = (u32x2_){w0, w1}; }
;                 else { u32x4 w; w.x = cvt_pk_bf16(o[0], o[1]); w.y = cvt_pk_bf16(o[2], o[3]); w.z = cvt_pk_bf16(o[4], o[5]); w.w = cvt_pk_bf16(o[6], o[7]);
;                     __builtin_nontemporal_store(w, (u32x4*)((bf16_t*)O + off)); } }
	global_store_dwordx4 v[116:117], v[120:123], off nt
	v_mul_f32_e32 v126, v124, v119
	v_exp_f32_e32 v126, v126
	v_mul_f32_e32 v121, v125, v119
	v_exp_f32_e32 v121, v121
	v_pk_mul_f32 v[112:113], v[144:145], v[112:113]
	v_add_f32_e32 v120, 1.0, v126
	v_rcp_f32_e32 v120, v120
	v_add_f32_e32 v121, 1.0, v121
	v_rcp_f32_e32 v121, v121
	v_mul_f32_e32 v122, v112, v119
	v_exp_f32_e32 v122, v122
	v_or_b32_e32 v117, 16, v168
	v_mul_f32_e32 v116, v175, v175
	v_pk_mul_f32 v[106:107], v[138:139], v[106:107]
	v_pk_mul_f32 v[120:121], v[116:117], v[120:121] op_sel_hi:[0,1]
	v_pk_mul_f32 v[106:107], v[124:125], v[106:107]
	v_pk_mul_f32 v[108:109], v[140:141], v[108:109]
	v_pk_mul_f32 v[106:107], v[106:107], v[120:121]
	v_pk_mul_f32 v[108:109], v[112:113], v[108:109]
	v_cvt_pk_bf16_f32 v106, v106, v107
	v_add_f32_e32 v107, 1.0, v122
	v_rcp_f32_e32 v120, v107
	v_mul_f32_e32 v107, v113, v119
	v_exp_f32_e32 v107, v107
	v_pk_mul_f32 v[102:103], v[134:135], v[102:103]
	v_pk_mul_f32 v[98:99], v[130:131], v[98:99]
	v_pk_mul_f32 v[104:105], v[136:137], v[104:105]
	v_add_f32_e32 v107, 1.0, v107
	v_rcp_f32_e32 v121, v107
	v_mul_f32_e32 v107, v102, v119
	v_exp_f32_e32 v122, v107
	v_pk_mul_f32 v[98:99], v[102:103], v[98:99]
	v_pk_mul_f32 v[112:113], v[116:117], v[120:121] op_sel_hi:[0,1]
	v_pk_mul_f32 v[108:109], v[108:109], v[112:113]
	v_mul_f32_e32 v112, v104, v119
	v_cvt_pk_bf16_f32 v107, v108, v109
	v_mul_f32_e32 v109, v103, v119
	v_exp_f32_e32 v109, v109
	v_add_f32_e32 v108, 1.0, v122
	v_rcp_f32_e32 v108, v108
	v_exp_f32_e32 v112, v112
	v_add_f32_e32 v109, 1.0, v109
	v_rcp_f32_e32 v109, v109
	v_pk_mul_f32 v[94:95], v[142:143], v[94:95]
	v_pk_mul_f32 v[90:91], v[138:139], v[90:91]
	v_pk_mul_f32 v[92:93], v[140:141], v[92:93]
	v_pk_mul_f32 v[102:103], v[116:117], v[108:109] op_sel_hi:[0,1]
	v_pk_mul_f32 v[98:99], v[98:99], v[102:103]
	v_mul_f32_e32 v103, v105, v119
	v_exp_f32_e32 v103, v103
	v_add_f32_e32 v102, 1.0, v112
	v_rcp_f32_e32 v102, v102
	v_cvt_pk_bf16_f32 v108, v98, v99
	v_add_f32_e32 v103, 1.0, v103
	v_rcp_f32_e32 v103, v103
	v_pk_mul_f32 v[98:99], v[132:133], v[100:101]
	v_pk_mul_f32 v[90:91], v[94:95], v[90:91]
	v_pk_mul_f32 v[98:99], v[104:105], v[98:99]
	v_pk_mul_f32 v[100:101], v[116:117], v[102:103] op_sel_hi:[0,1]
	v_pk_mul_f32 v[98:99], v[98:99], v[100:101]
	v_mad_i64_i32 v[100:101], s[24:25], v117, s62, v[114:115]
	v_cvt_pk_bf16_f32 v109, v98, v99
	ds_read2_b32 v[98:99], v118 offset0:32 offset1:48
	v_lshl_add_u64 v[100:101], v[100:101], 0, v[110:111]
	global_store_dwordx4 v[100:101], v[106:109], off nt
	v_pk_mul_f32 v[86:87], v[134:135], v[86:87]
	v_pk_mul_f32 v[82:83], v[130:131], v[82:83]
	s_waitcnt lgkmcnt(0)
	v_mul_f32_e32 v102, 0xbfb8aa3b, v98
	v_mul_f32_e32 v103, v94, v102
	v_mul_f32_e32 v101, v95, v102
	v_exp_f32_e32 v103, v103
	v_exp_f32_e32 v101, v101
	v_pk_mul_f32 v[94:95], v[144:145], v[96:97]
	v_mul_f32_e32 v98, v98, v98
	v_add_f32_e32 v100, 1.0, v103
	v_add_f32_e32 v101, 1.0, v101
	v_rcp_f32_e32 v100, v100
	v_rcp_f32_e32 v101, v101
	v_mul_f32_e32 v96, v94, v102
	v_exp_f32_e32 v103, v96
	v_pk_mul_f32 v[92:93], v[94:95], v[92:93]
	v_pk_mul_f32 v[96:97], v[98:99], v[100:101] op_sel_hi:[0,1]
	v_pk_mul_f32 v[90:91], v[90:91], v[96:97]
	v_pk_mul_f32 v[88:89], v[136:137], v[88:89]
	v_cvt_pk_bf16_f32 v90, v90, v91
	v_add_f32_e32 v91, 1.0, v103
	v_rcp_f32_e32 v96, v91
	v_mul_f32_e32 v91, v95, v102
	v_exp_f32_e32 v91, v91
	v_pk_mul_f32 v[82:83], v[86:87], v[82:83]
	v_cvt_f32_i32_e32 v85, v85
	v_cvt_f32_i32_e32 v84, v84
	v_add_f32_e32 v91, 1.0, v91
	v_rcp_f32_e32 v97, v91
	v_mul_f32_e32 v91, v86, v102
	v_exp_f32_e32 v100, v91
	v_cvt_f32_i32_e32 v79, v79
	v_pk_mul_f32 v[94:95], v[98:99], v[96:97] op_sel_hi:[0,1]
	v_pk_mul_f32 v[92:93], v[92:93], v[94:95]
	v_mul_f32_e32 v94, v88, v102
	v_cvt_pk_bf16_f32 v91, v92, v93
	v_mul_f32_e32 v93, v87, v102
	v_exp_f32_e32 v93, v93
	v_add_f32_e32 v92, 1.0, v100
	v_rcp_f32_e32 v92, v92
	v_exp_f32_e32 v94, v94
	v_add_f32_e32 v93, 1.0, v93
	v_rcp_f32_e32 v93, v93
	v_cvt_f32_i32_e32 v78, v78
	v_cvt_f32_i32_e32 v75, v75
	v_cvt_f32_i32_e32 v74, v74
	v_pk_mul_f32 v[86:87], v[98:99], v[92:93] op_sel_hi:[0,1]
	v_pk_mul_f32 v[82:83], v[82:83], v[86:87]
	v_mul_f32_e32 v87, v89, v102
	v_exp_f32_e32 v87, v87
	v_add_f32_e32 v86, 1.0, v94
	v_rcp_f32_e32 v86, v86
	v_cvt_pk_bf16_f32 v92, v82, v83
	v_add_f32_e32 v87, 1.0, v87
	v_rcp_f32_e32 v87, v87
	v_pk_mul_f32 v[82:83], v[132:133], v[84:85]
	v_pk_mul_f32 v[78:79], v[142:143], v[78:79]
	v_pk_mul_f32 v[82:83], v[88:89], v[82:83]
	v_pk_mul_f32 v[84:85], v[98:99], v[86:87] op_sel_hi:[0,1]
	v_mul_f32_e32 v86, 0xbfb8aa3b, v99
	v_pk_mul_f32 v[82:83], v[82:83], v[84:85]
	v_mul_f32_e32 v84, v78, v86
	v_mul_f32_e32 v85, v79, v86
	v_exp_f32_e32 v84, v84
	v_exp_f32_e32 v85, v85
	v_cvt_f32_i32_e32 v81, v81
	v_cvt_f32_i32_e32 v80, v80
	v_add_f32_e32 v84, 1.0, v84
	v_pk_mul_f32 v[74:75], v[138:139], v[74:75]
	v_add_f32_e32 v85, 1.0, v85
	v_or_b32_e32 v104, 32, v168
	v_rcp_f32_e32 v84, v84
	v_rcp_f32_e32 v85, v85
	v_pk_mul_f32 v[74:75], v[78:79], v[74:75]
	v_pk_mul_f32 v[78:79], v[144:145], v[80:81]
	v_cvt_pk_bf16_f32 v93, v82, v83
	v_mad_i64_i32 v[82:83], s[24:25], v104, s62, v[114:115]
	v_mul_f32_e32 v80, v78, v86
	v_lshl_add_u64 v[82:83], v[82:83], 0, v[110:111]
	v_exp_f32_e32 v87, v80
	global_store_dwordx4 v[82:83], v[90:93], off nt
	v_or_b32_e32 v83, 48, v168
	v_mul_f32_e32 v82, v99, v99
	v_pk_mul_f32 v[80:81], v[82:83], v[84:85] op_sel_hi:[0,1]
	v_pk_mul_f32 v[74:75], v[74:75], v[80:81]
	v_cvt_f32_i32_e32 v77, v77
	v_cvt_pk_bf16_f32 v74, v74, v75
	v_add_f32_e32 v75, 1.0, v87
	v_rcp_f32_e32 v80, v75
	v_mul_f32_e32 v75, v79, v86
	v_exp_f32_e32 v75, v75
	v_cvt_f32_i32_e32 v76, v76
; __device__ __forceinline__ float fast_sigmoid(float x) { return __builtin_amdgcn_rcpf(1.0f + __expf(-x)); }
;     __device__ __forceinline__ void operator()(const f32x4 (&acc)[2][2][4][2], const Unit& u, int wr, int wc, int fr, int fq) const {
;     ...
;             for (int m = 0; m < 4; ++m) { const size_t off = (size_t)(row0 + ai * HALF + m * 16) * ldc + col0;
;                 const float rs = IN8 ? rt.tab[sl * 256 + wr * 64 + ai * HALF + m * 16 + fr] : isc;
;                 const float rsn = rs * -1.4426950408889634f, rs2 = rs * rs; (void)rsn; (void)rs2;
;                 float o[8];
; #pragma unroll
;                 for (int n = 0; n < 2; ++n)
; #pragma unroll
;                     for (int e = 0; e < 4; ++e) { const float ga = acc[ai][0][m][n][e], ua = acc[ai][1][m][n][e];
;                         if (IN8) {
;                             const float gq = (float)__float_as_int(ga) * cg[n][e], uq = (float)__float_as_int(ua) * cu[n][e];
;                             const float sg = __builtin_amdgcn_rcpf(1.0f + __builtin_amdgcn_exp2f(gq * rsn));
;                             o[4 * n + e] = (gq * uq) * (sg * rs2); }
;                         else { const float g = ga * rs, up = ua * rs; o[4 * n + e] = g * fast_sigmoid(g) * up; } }
;                 if (F8) { unsigned w0 = 0u, w1 = 0u;
; #pragma unroll
;                     for (int e = 0; e < 8; ++e) o[e] = __builtin_amdgcn_fmed3f(o[e] * H8_SCALE, -448.0f, 448.0f);
;                     w0 = __builtin_amdgcn_cvt_pk_fp8_f32(o[0], o[1], w0, false); w0 = __builtin_amdgcn_cvt_pk_fp8_f32(o[2], o[3], w0, true);
;                     w1 = __builtin_amdgcn_cvt_pk_fp8_f32(o[4], o[5], w1, false); w1 = __builtin_amdgcn_cvt_pk_fp8_f32(o[6], o[7], w1, true);
;                     typedef unsigned u32x2_ __attribute__((ext_vector_type(2))); *(u32x2_*)((unsigned char*)O + off) = (u32x2_){w0, w1}; }
;                 else { u32x4 w; w.x = cvt_pk_bf16(o[0], o[1]); w.y = cvt_pk_bf16(o[2], o[3]); w.z = cvt_pk_bf16(o[4], o[5]); w.w = cvt_pk_bf16(o[6], o[7]);
;                     __builtin_nontemporal_store(w, (u32x4*)((bf16_t*)O + off)); } }
	v_cvt_f32_i32_e32 v71, v71
	v_cvt_f32_i32_e32 v70, v70
	v_add_f32_e32 v75, 1.0, v75
	v_rcp_f32_e32 v81, v75
	v_pk_mul_f32 v[76:77], v[140:141], v[76:77]
	v_pk_mul_f32 v[70:71], v[134:135], v[70:71]
	v_pk_mul_f32 v[76:77], v[78:79], v[76:77]
	v_pk_mul_f32 v[78:79], v[82:83], v[80:81] op_sel_hi:[0,1]
	v_mul_f32_e32 v75, v70, v86
	v_pk_mul_f32 v[76:77], v[76:77], v[78:79]
	v_exp_f32_e32 v84, v75
	v_cvt_pk_bf16_f32 v75, v76, v77
	v_mul_f32_e32 v77, v71, v86
	v_exp_f32_e32 v77, v77
	v_add_f32_e32 v76, 1.0, v84
	v_cvt_f32_i32_e32 v67, v67
	v_cvt_f32_i32_e32 v66, v66
	v_add_f32_e32 v77, 1.0, v77
	v_rcp_f32_e32 v76, v76
	v_cvt_f32_i32_e32 v73, v73
	v_cvt_f32_i32_e32 v72, v72
	v_rcp_f32_e32 v77, v77
	v_pk_mul_f32 v[66:67], v[130:131], v[66:67]
	v_cvt_f32_i32_e32 v69, v69
	v_pk_mul_f32 v[72:73], v[136:137], v[72:73]
	v_pk_mul_f32 v[66:67], v[70:71], v[66:67]
	v_pk_mul_f32 v[70:71], v[82:83], v[76:77] op_sel_hi:[0,1]
	v_mul_f32_e32 v78, v72, v86
	v_pk_mul_f32 v[66:67], v[66:67], v[70:71]
	v_mul_f32_e32 v71, v73, v86
	v_exp_f32_e32 v78, v78
	v_exp_f32_e32 v71, v71
	v_cvt_f32_i32_e32 v68, v68
	v_cvt_pk_bf16_f32 v76, v66, v67
	v_add_f32_e32 v70, 1.0, v78
	v_add_f32_e32 v71, 1.0, v71
	v_rcp_f32_e32 v70, v70
	v_rcp_f32_e32 v71, v71
	v_pk_mul_f32 v[66:67], v[132:133], v[68:69]
	v_cvt_f32_i32_e32 v63, v63
	v_pk_mul_f32 v[66:67], v[72:73], v[66:67]
	v_pk_mul_f32 v[68:69], v[82:83], v[70:71] op_sel_hi:[0,1]
	v_pk_mul_f32 v[66:67], v[66:67], v[68:69]
	v_cvt_f32_i32_e32 v62, v62
	v_cvt_pk_bf16_f32 v77, v66, v67
	ds_read2_b32 v[66:67], v118 offset0:128 offset1:144
	v_mad_i64_i32 v[68:69], s[24:25], v83, s62, v[114:115]
	v_lshl_add_u64 v[68:69], v[68:69], 0, v[110:111]
	v_pk_mul_f32 v[62:63], v[142:143], v[62:63]
	s_waitcnt lgkmcnt(0)
	v_mul_f32_e32 v70, 0xbfb8aa3b, v66
	v_mul_f32_e32 v71, v62, v70
	global_store_dwordx4 v[68:69], v[74:77], off nt
	v_mul_f32_e32 v69, v63, v70
	v_exp_f32_e32 v71, v71
	v_cvt_f32_i32_e32 v59, v59
	v_cvt_f32_i32_e32 v58, v58
	v_exp_f32_e32 v69, v69
	v_cvt_f32_i32_e32 v65, v65
	v_cvt_f32_i32_e32 v64, v64
	v_add_f32_e32 v68, 1.0, v71
	v_pk_mul_f32 v[58:59], v[138:139], v[58:59]
	v_add_f32_e32 v69, 1.0, v69
	v_rcp_f32_e32 v68, v68
	v_rcp_f32_e32 v69, v69
	v_pk_mul_f32 v[58:59], v[62:63], v[58:59]
	v_pk_mul_f32 v[62:63], v[144:145], v[64:65]
	v_mul_f32_e32 v66, v66, v66
	v_mul_f32_e32 v64, v62, v70
	v_exp_f32_e32 v71, v64
	v_pk_mul_f32 v[64:65], v[66:67], v[68:69] op_sel_hi:[0,1]
	v_pk_mul_f32 v[58:59], v[58:59], v[64:65]
	v_cvt_f32_i32_e32 v61, v61
	v_cvt_pk_bf16_f32 v58, v58, v59
	v_add_f32_e32 v59, 1.0, v71
	v_rcp_f32_e32 v64, v59
	v_mul_f32_e32 v59, v63, v70
	v_exp_f32_e32 v59, v59
	v_cvt_f32_i32_e32 v60, v60
	v_cvt_f32_i32_e32 v55, v55
	v_cvt_f32_i32_e32 v54, v54
	v_add_f32_e32 v59, 1.0, v59
	v_rcp_f32_e32 v65, v59
	v_pk_mul_f32 v[60:61], v[140:141], v[60:61]
	v_pk_mul_f32 v[54:55], v[134:135], v[54:55]
	v_pk_mul_f32 v[60:61], v[62:63], v[60:61]
	v_pk_mul_f32 v[62:63], v[66:67], v[64:65] op_sel_hi:[0,1]
	v_mul_f32_e32 v59, v54, v70
	v_pk_mul_f32 v[60:61], v[60:61], v[62:63]
	v_exp_f32_e32 v68, v59
	v_cvt_pk_bf16_f32 v59, v60, v61
	v_mul_f32_e32 v61, v55, v70
	v_exp_f32_e32 v61, v61
	v_add_f32_e32 v60, 1.0, v68
	v_cvt_f32_i32_e32 v51, v51
	v_cvt_f32_i32_e32 v50, v50
	v_add_f32_e32 v61, 1.0, v61
	v_rcp_f32_e32 v60, v60
	v_cvt_f32_i32_e32 v57, v57
	v_cvt_f32_i32_e32 v56, v56
	v_rcp_f32_e32 v61, v61
	v_pk_mul_f32 v[50:51], v[130:131], v[50:51]
	v_cvt_f32_i32_e32 v53, v53
	v_pk_mul_f32 v[56:57], v[136:137], v[56:57]
	v_pk_mul_f32 v[50:51], v[54:55], v[50:51]
	v_pk_mul_f32 v[54:55], v[66:67], v[60:61] op_sel_hi:[0,1]
	v_mul_f32_e32 v62, v56, v70
	v_pk_mul_f32 v[50:51], v[50:51], v[54:55]
	v_mul_f32_e32 v55, v57, v70
	v_exp_f32_e32 v62, v62
	v_exp_f32_e32 v55, v55
	v_cvt_f32_i32_e32 v52, v52
	v_cvt_f32_i32_e32 v47, v47
	v_add_f32_e32 v54, 1.0, v62
	v_add_f32_e32 v55, 1.0, v55
	v_rcp_f32_e32 v54, v54
	v_rcp_f32_e32 v55, v55
	v_cvt_f32_i32_e32 v46, v46
	v_cvt_pk_bf16_f32 v60, v50, v51
	v_pk_mul_f32 v[50:51], v[132:133], v[52:53]
	v_pk_mul_f32 v[52:53], v[66:67], v[54:55] op_sel_hi:[0,1]
	v_pk_mul_f32 v[50:51], v[56:57], v[50:51]
	v_mul_f32_e32 v54, 0xbfb8aa3b, v67
	v_pk_mul_f32 v[46:47], v[142:143], v[46:47]
	v_pk_mul_f32 v[50:51], v[50:51], v[52:53]
	v_mul_f32_e32 v52, v46, v54
	v_mul_f32_e32 v53, v47, v54
	v_exp_f32_e32 v52, v52
	v_cvt_f32_i32_e32 v43, v43
	v_cvt_f32_i32_e32 v42, v42
	v_exp_f32_e32 v53, v53
	v_cvt_f32_i32_e32 v49, v49
	v_cvt_f32_i32_e32 v48, v48
	v_add_f32_e32 v52, 1.0, v52
	v_pk_mul_f32 v[42:43], v[138:139], v[42:43]
	v_add_f32_e32 v53, 1.0, v53
	v_add_u32_e32 v72, 0x80, v168
	v_rcp_f32_e32 v52, v52
	v_rcp_f32_e32 v53, v53
	v_pk_mul_f32 v[42:43], v[46:47], v[42:43]
	v_pk_mul_f32 v[46:47], v[144:145], v[48:49]
	v_cvt_pk_bf16_f32 v61, v50, v51
	v_mad_i64_i32 v[50:51], s[24:25], v72, s62, v[114:115]
	v_mul_f32_e32 v48, v46, v54
	v_lshl_add_u64 v[50:51], v[50:51], 0, v[110:111]
	v_exp_f32_e32 v55, v48
	global_store_dwordx4 v[50:51], v[58:61], off nt
	v_add_u32_e32 v51, 0x90, v168
	v_mul_f32_e32 v50, v67, v67
	v_pk_mul_f32 v[48:49], v[50:51], v[52:53] op_sel_hi:[0,1]
	v_pk_mul_f32 v[42:43], v[42:43], v[48:49]
	v_cvt_f32_i32_e32 v45, v45
	v_cvt_pk_bf16_f32 v42, v42, v43
	v_add_f32_e32 v43, 1.0, v55
	v_rcp_f32_e32 v48, v43
	v_mul_f32_e32 v43, v47, v54
	v_exp_f32_e32 v43, v43
	v_cvt_f32_i32_e32 v44, v44
	v_cvt_f32_i32_e32 v39, v39
	v_cvt_f32_i32_e32 v38, v38
	v_add_f32_e32 v43, 1.0, v43
	v_rcp_f32_e32 v49, v43
	v_pk_mul_f32 v[44:45], v[140:141], v[44:45]
	v_pk_mul_f32 v[38:39], v[134:135], v[38:39]
	v_pk_mul_f32 v[44:45], v[46:47], v[44:45]
	v_pk_mul_f32 v[46:47], v[50:51], v[48:49] op_sel_hi:[0,1]
	v_mul_f32_e32 v43, v38, v54
; __device__ __forceinline__ float fast_sigmoid(float x) { return __builtin_amdgcn_rcpf(1.0f + __expf(-x)); }
;     __device__ __forceinline__ void operator()(const f32x4 (&acc)[2][2][4][2], const Unit& u, int wr, int wc, int fr, int fq) const {
;     ...
;             for (int m = 0; m < 4; ++m) { const size_t off = (size_t)(row0 + ai * HALF + m * 16) * ldc + col0;
;                 const float rs = IN8 ? rt.tab[sl * 256 + wr * 64 + ai * HALF + m * 16 + fr] : isc;
;                 const float rsn = rs * -1.4426950408889634f, rs2 = rs * rs; (void)rsn; (void)rs2;
;                 float o[8];
; #pragma unroll
;                 for (int n = 0; n < 2; ++n)
; #pragma unroll
;                     for (int e = 0; e < 4; ++e) { const float ga = acc[ai][0][m][n][e], ua = acc[ai][1][m][n][e];
;                         if (IN8) {
;                             const float gq = (float)__float_as_int(ga) * cg[n][e], uq = (float)__float_as_int(ua) * cu[n][e];
;                             const float sg = __builtin_amdgcn_rcpf(1.0f + __builtin_amdgcn_exp2f(gq * rsn));
;                             o[4 * n + e] = (gq * uq) * (sg * rs2); }
;                         else { const float g = ga * rs, up = ua * rs; o[4 * n + e] = g * fast_sigmoid(g) * up; } }
;                 if (F8) { unsigned w0 = 0u, w1 = 0u;
; #pragma unroll
;                     for (int e = 0; e < 8; ++e) o[e] = __builtin_amdgcn_fmed3f(o[e] * H8_SCALE, -448.0f, 448.0f);
;                     w0 = __builtin_amdgcn_cvt_pk_fp8_f32(o[0], o[1], w0, false); w0 = __builtin_amdgcn_cvt_pk_fp8_f32(o[2], o[3], w0, true);
;                     w1 = __builtin_amdgcn_cvt_pk_fp8_f32(o[4], o[5], w1, false); w1 = __builtin_amdgcn_cvt_pk_fp8_f32(o[6], o[7], w1, true);
;                     typedef unsigned u32x2_ __attribute__((ext_vector_type(2))); *(u32x2_*)((unsigned char*)O + off) = (u32x2_){w0, w1}; }
;                 else { u32x4 w; w.x = cvt_pk_bf16(o[0], o[1]); w.y = cvt_pk_bf16(o[2], o[3]); w.z = cvt_pk_bf16(o[4], o[5]); w.w = cvt_pk_bf16(o[6], o[7]);
;                     __builtin_nontemporal_store(w, (u32x4*)((bf16_t*)O + off)); } }
;     ...
;         if (!has_next) break;
	v_pk_mul_f32 v[44:45], v[44:45], v[46:47]
	v_exp_f32_e32 v52, v43
	v_cvt_pk_bf16_f32 v43, v44, v45
	v_mul_f32_e32 v45, v39, v54
	v_exp_f32_e32 v45, v45
	v_add_f32_e32 v44, 1.0, v52
	v_cvt_f32_i32_e32 v35, v35
	v_cvt_f32_i32_e32 v34, v34
	v_add_f32_e32 v45, 1.0, v45
	v_rcp_f32_e32 v44, v44
	v_cvt_f32_i32_e32 v41, v41
	v_cvt_f32_i32_e32 v40, v40
	v_rcp_f32_e32 v45, v45
	v_pk_mul_f32 v[34:35], v[130:131], v[34:35]
	v_cvt_f32_i32_e32 v37, v37
	v_pk_mul_f32 v[40:41], v[136:137], v[40:41]
	v_pk_mul_f32 v[34:35], v[38:39], v[34:35]
	v_pk_mul_f32 v[38:39], v[50:51], v[44:45] op_sel_hi:[0,1]
	v_mul_f32_e32 v46, v40, v54
	v_pk_mul_f32 v[34:35], v[34:35], v[38:39]
	v_mul_f32_e32 v39, v41, v54
	v_exp_f32_e32 v46, v46
	v_exp_f32_e32 v39, v39
	v_cvt_f32_i32_e32 v36, v36
	v_cvt_pk_bf16_f32 v44, v34, v35
	v_add_f32_e32 v38, 1.0, v46
	v_add_f32_e32 v39, 1.0, v39
	v_rcp_f32_e32 v38, v38
	v_rcp_f32_e32 v39, v39
	v_pk_mul_f32 v[34:35], v[132:133], v[36:37]
	v_cvt_f32_i32_e32 v31, v31
	v_pk_mul_f32 v[34:35], v[40:41], v[34:35]
	v_pk_mul_f32 v[36:37], v[50:51], v[38:39] op_sel_hi:[0,1]
	v_pk_mul_f32 v[34:35], v[34:35], v[36:37]
	v_cvt_f32_i32_e32 v30, v30
	v_cvt_pk_bf16_f32 v45, v34, v35
	ds_read2_b32 v[34:35], v118 offset0:160 offset1:176
	v_mad_i64_i32 v[36:37], s[24:25], v51, s62, v[114:115]
	v_lshl_add_u64 v[36:37], v[36:37], 0, v[110:111]
	v_pk_mul_f32 v[30:31], v[142:143], v[30:31]
	s_waitcnt lgkmcnt(0)
	v_mul_f32_e32 v38, 0xbfb8aa3b, v34
	v_mul_f32_e32 v39, v30, v38
	global_store_dwordx4 v[36:37], v[42:45], off nt
	v_mul_f32_e32 v37, v31, v38
	v_exp_f32_e32 v39, v39
	v_cvt_f32_i32_e32 v27, v27
	v_cvt_f32_i32_e32 v26, v26
	v_exp_f32_e32 v37, v37
	v_cvt_f32_i32_e32 v33, v33
	v_cvt_f32_i32_e32 v32, v32
	v_add_f32_e32 v36, 1.0, v39
	v_pk_mul_f32 v[26:27], v[138:139], v[26:27]
	v_add_f32_e32 v37, 1.0, v37
	v_rcp_f32_e32 v36, v36
	v_rcp_f32_e32 v37, v37
	v_pk_mul_f32 v[26:27], v[30:31], v[26:27]
	v_pk_mul_f32 v[30:31], v[144:145], v[32:33]
	v_mul_f32_e32 v34, v34, v34
	v_mul_f32_e32 v32, v30, v38
	v_exp_f32_e32 v39, v32
	v_pk_mul_f32 v[32:33], v[34:35], v[36:37] op_sel_hi:[0,1]
	v_pk_mul_f32 v[26:27], v[26:27], v[32:33]
	v_cvt_f32_i32_e32 v29, v29
	v_cvt_pk_bf16_f32 v26, v26, v27
	v_add_f32_e32 v27, 1.0, v39
	v_rcp_f32_e32 v32, v27
	v_mul_f32_e32 v27, v31, v38
	v_exp_f32_e32 v27, v27
	v_cvt_f32_i32_e32 v28, v28
	v_cvt_f32_i32_e32 v23, v23
	v_cvt_f32_i32_e32 v22, v22
	v_add_f32_e32 v27, 1.0, v27
	v_rcp_f32_e32 v33, v27
	v_pk_mul_f32 v[28:29], v[140:141], v[28:29]
	v_pk_mul_f32 v[22:23], v[134:135], v[22:23]
	v_pk_mul_f32 v[28:29], v[30:31], v[28:29]
	v_pk_mul_f32 v[30:31], v[34:35], v[32:33] op_sel_hi:[0,1]
	v_mul_f32_e32 v27, v22, v38
	v_pk_mul_f32 v[28:29], v[28:29], v[30:31]
	v_exp_f32_e32 v36, v27
	v_cvt_pk_bf16_f32 v27, v28, v29
	v_mul_f32_e32 v29, v23, v38
	v_exp_f32_e32 v29, v29
	v_add_f32_e32 v28, 1.0, v36
	v_cvt_f32_i32_e32 v19, v19
	v_cvt_f32_i32_e32 v18, v18
	v_add_f32_e32 v29, 1.0, v29
	v_rcp_f32_e32 v28, v28
	v_cvt_f32_i32_e32 v25, v25
	v_cvt_f32_i32_e32 v24, v24
	v_rcp_f32_e32 v29, v29
	v_pk_mul_f32 v[18:19], v[130:131], v[18:19]
	v_cvt_f32_i32_e32 v21, v21
	v_pk_mul_f32 v[24:25], v[136:137], v[24:25]
	v_pk_mul_f32 v[18:19], v[22:23], v[18:19]
	v_pk_mul_f32 v[22:23], v[34:35], v[28:29] op_sel_hi:[0,1]
	v_mul_f32_e32 v30, v24, v38
	v_pk_mul_f32 v[18:19], v[18:19], v[22:23]
	v_mul_f32_e32 v23, v25, v38
	v_exp_f32_e32 v30, v30
	v_exp_f32_e32 v23, v23
	v_cvt_f32_i32_e32 v20, v20
	v_cvt_f32_i32_e32 v15, v15
	v_add_f32_e32 v22, 1.0, v30
	v_add_f32_e32 v23, 1.0, v23
	v_rcp_f32_e32 v22, v22
	v_rcp_f32_e32 v23, v23
	v_cvt_f32_i32_e32 v14, v14
	v_cvt_pk_bf16_f32 v28, v18, v19
	v_pk_mul_f32 v[18:19], v[132:133], v[20:21]
	v_pk_mul_f32 v[20:21], v[34:35], v[22:23] op_sel_hi:[0,1]
	v_pk_mul_f32 v[18:19], v[24:25], v[18:19]
	v_mul_f32_e32 v22, 0xbfb8aa3b, v35
	v_pk_mul_f32 v[14:15], v[142:143], v[14:15]
	v_pk_mul_f32 v[18:19], v[18:19], v[20:21]
	v_mul_f32_e32 v20, v14, v22
	v_mul_f32_e32 v21, v15, v22
	v_exp_f32_e32 v20, v20
	v_cvt_f32_i32_e32 v11, v11
	v_cvt_f32_i32_e32 v10, v10
	v_exp_f32_e32 v21, v21
	v_cvt_f32_i32_e32 v17, v17
	v_cvt_f32_i32_e32 v16, v16
	v_add_f32_e32 v20, 1.0, v20
	v_pk_mul_f32 v[10:11], v[138:139], v[10:11]
	v_add_f32_e32 v21, 1.0, v21
	v_add_u32_e32 v40, 0xa0, v168
	v_rcp_f32_e32 v20, v20
	v_rcp_f32_e32 v21, v21
	v_pk_mul_f32 v[10:11], v[14:15], v[10:11]
	v_pk_mul_f32 v[14:15], v[144:145], v[16:17]
	v_cvt_pk_bf16_f32 v29, v18, v19
	v_mad_i64_i32 v[18:19], s[24:25], v40, s62, v[114:115]
	v_mul_f32_e32 v16, v14, v22
	v_lshl_add_u64 v[18:19], v[18:19], 0, v[110:111]
	v_exp_f32_e32 v23, v16
	global_store_dwordx4 v[18:19], v[26:29], off nt
	v_add_u32_e32 v19, 0xb0, v168
	v_mul_f32_e32 v18, v35, v35
	v_pk_mul_f32 v[16:17], v[18:19], v[20:21] op_sel_hi:[0,1]
	v_pk_mul_f32 v[10:11], v[10:11], v[16:17]
	v_cvt_f32_i32_e32 v13, v13
	v_cvt_pk_bf16_f32 v10, v10, v11
	v_add_f32_e32 v11, 1.0, v23
	v_rcp_f32_e32 v16, v11
	v_mul_f32_e32 v11, v15, v22
	v_exp_f32_e32 v11, v11
	v_cvt_f32_i32_e32 v12, v12
	v_cvt_f32_i32_e32 v7, v7
	v_cvt_f32_i32_e32 v6, v6
	v_add_f32_e32 v11, 1.0, v11
	v_rcp_f32_e32 v17, v11
	v_pk_mul_f32 v[12:13], v[140:141], v[12:13]
	v_pk_mul_f32 v[6:7], v[134:135], v[6:7]
	v_pk_mul_f32 v[12:13], v[14:15], v[12:13]
	v_pk_mul_f32 v[14:15], v[18:19], v[16:17] op_sel_hi:[0,1]
	v_mul_f32_e32 v11, v6, v22
	v_pk_mul_f32 v[12:13], v[12:13], v[14:15]
	v_exp_f32_e32 v20, v11
	v_cvt_pk_bf16_f32 v11, v12, v13
	v_mul_f32_e32 v13, v7, v22
	v_exp_f32_e32 v13, v13
	v_add_f32_e32 v12, 1.0, v20
	v_cvt_f32_i32_e32 v3, v3
	v_cvt_f32_i32_e32 v2, v2
	v_add_f32_e32 v13, 1.0, v13
	v_rcp_f32_e32 v12, v12
	v_cvt_f32_i32_e32 v9, v9
	v_cvt_f32_i32_e32 v8, v8
	v_rcp_f32_e32 v13, v13
	v_pk_mul_f32 v[2:3], v[130:131], v[2:3]
	v_cvt_f32_i32_e32 v5, v5
	v_pk_mul_f32 v[8:9], v[136:137], v[8:9]
	v_pk_mul_f32 v[2:3], v[6:7], v[2:3]
	v_pk_mul_f32 v[6:7], v[18:19], v[12:13] op_sel_hi:[0,1]
	v_mul_f32_e32 v14, v8, v22
	v_pk_mul_f32 v[2:3], v[2:3], v[6:7]
	v_mul_f32_e32 v7, v9, v22
	v_exp_f32_e32 v14, v14
	v_exp_f32_e32 v7, v7
	v_cvt_f32_i32_e32 v4, v4
	v_cvt_pk_bf16_f32 v12, v2, v3
	v_add_f32_e32 v6, 1.0, v14
	v_add_f32_e32 v7, 1.0, v7
	v_rcp_f32_e32 v6, v6
	v_rcp_f32_e32 v7, v7
	v_pk_mul_f32 v[2:3], v[132:133], v[4:5]
	s_andn2_b64 vcc, exec, s[0:1]
	v_pk_mul_f32 v[2:3], v[8:9], v[2:3]
	v_pk_mul_f32 v[4:5], v[18:19], v[6:7] op_sel_hi:[0,1]
	v_pk_mul_f32 v[2:3], v[2:3], v[4:5]
	s_mov_b64 s[0:1], -1
	v_cvt_pk_bf16_f32 v13, v2, v3
	v_mad_i64_i32 v[2:3], s[24:25], v19, s62, v[114:115]
	v_lshl_add_u64 v[2:3], v[2:3], 0, v[110:111]
	global_store_dwordx4 v[2:3], v[10:13], off nt
	s_cbranch_vccnz .LBB0_222
	s_andn2_b64 vcc, exec, s[4:5]
	s_cbranch_vccnz .LBB0_221
	s_barrier
	s_branch .LBB0_221
